# dense loop: e4m3 packing of the pending tile hoisted in front of the row-sum check (redone on rescale), V fragment 1 read during the QK phase, staging writes behind the K fragment reads
# baseline (speedup 1.0000x reference)
.LBB0_409:
	s_waitcnt vmcnt(0)
	ds_read_b128 v[68:71], v192 offset:49152
	ds_read_b128 v[72:75], v193 offset:49152
	ds_read_b128 v[208:211], v194 offset:49152
	ds_read_b128 v[212:215], v195 offset:49152
	ds_read_b128 v[200:203], v192 offset:53248
	ds_read_b128 v[204:207], v193 offset:53248
	v_mov_b32_e32 v254, v116
	v_mov_b32_e32 v255, v118
	ds_write_b64 v189, v[254:255] offset:8192
	v_mov_b32_e32 v244, v117
	v_mov_b32_e32 v245, v119
	ds_write_b64 v190, v[244:245] offset:8192
	ds_write_b128 v191, v[120:123] offset:40960
	v_cvt_pk_fp8_f32 v232, v173, v177
	v_cvt_pk_fp8_f32 v233, v174, v178
	v_cvt_pk_fp8_f32 v234, v175, v179
	v_cvt_pk_fp8_f32 v235, v176, v180
	v_cvt_pk_fp8_f32 v232, v165, v166 op_sel:[0,0,1]
	v_cvt_pk_fp8_f32 v233, v167, v168 op_sel:[0,0,1]
	v_cvt_pk_fp8_f32 v234, v169, v170 op_sel:[0,0,1]
	s_waitcnt lgkmcnt(7)
	v_mfma_scale_f32_32x32x64_f8f6f4 v[84:99], v[68:75], v[100:107], v[216:231], v188, v247 op_sel_hi:[0,0,0]
	v_cvt_pk_fp8_f32 v235, v171, v172 op_sel:[0,0,1]
	v_cvt_pk_fp8_f32 v236, v154, v155
	v_cvt_pk_fp8_f32 v237, v128, v129
	v_cvt_pk_fp8_f32 v238, v124, v125
	v_cvt_pk_fp8_f32 v239, v158, v159
	v_cvt_pk_fp8_f32 v236, v130, v131 op_sel:[0,0,1]
	v_cvt_pk_fp8_f32 v237, v126, v127 op_sel:[0,0,1]
	v_cvt_pk_fp8_f32 v238, v160, v161 op_sel:[0,0,1]
	v_cvt_pk_fp8_f32 v239, v156, v157 op_sel:[0,0,1]
	v_add_f32_e32 v241, v154, v155
	v_add_f32_e32 v240, v173, v177
	s_waitcnt lgkmcnt(5)
	v_mfma_scale_f32_32x32x64_f8f6f4 v[84:99], v[208:215], v[108:115], v[84:99], v188, v247 op_sel_hi:[0,0,0]
	ds_read_b128 v[208:211], v197 offset:2048
	ds_read_b128 v[212:215], v198 offset:2048
	v_add_f32_e32 v241, v130, v241
	v_add_f32_e32 v240, v165, v240
	v_add_f32_e32 v241, v131, v241
	v_add_f32_e32 v240, v166, v240
	v_add_f32_e32 v241, v128, v241
	v_add_f32_e32 v240, v174, v240
	v_add_f32_e32 v241, v129, v241
	v_add_f32_e32 v240, v178, v240
	v_add_f32_e32 v241, v126, v241
	v_add_f32_e32 v240, v167, v240
	v_add_f32_e32 v241, v127, v241
	s_waitcnt lgkmcnt(5)
	v_mfma_scale_f32_32x32x64_f8f6f4 v[68:83], v[200:207], v[100:107], v[216:231], v188, v247 op_sel_hi:[0,0,0]
	ds_read_b128 v[200:203], v194 offset:53248
	ds_read_b128 v[204:207], v195 offset:53248
	v_add_f32_e32 v240, v168, v240
	v_add_f32_e32 v241, v124, v241
	v_add_f32_e32 v240, v175, v240
	v_add_f32_e32 v241, v125, v241
	v_add_f32_e32 v240, v179, v240
	v_add_f32_e32 v241, v160, v241
	v_add_f32_e32 v240, v169, v240
	v_add_f32_e32 v241, v161, v241
	v_add_f32_e32 v240, v170, v240
	v_add_f32_e32 v241, v158, v241
	v_add_f32_e32 v240, v176, v240
	v_add_f32_e32 v241, v159, v241
	s_waitcnt lgkmcnt(0)
	v_mfma_scale_f32_32x32x64_f8f6f4 v[68:83], v[200:207], v[108:115], v[68:83], v188, v247 op_sel_hi:[0,0,0]
	v_add_f32_e32 v240, v180, v240
	v_add_f32_e32 v241, v156, v241
	v_add_f32_e32 v240, v171, v240
	v_add_f32_e32 v241, v157, v241
	v_add_f32_e32 v240, v172, v240
	v_add_f32_e32 v162, v240, v241
	v_mov_b32_e32 v163, v162
	s_nop 0
	s_nop 0
	v_permlane32_swap_b32_e32 v162, v163
	v_add_f32_e32 v162, v162, v163
	v_cmp_ge_f32_e32 vcc, 0x43c80000, v162
	s_cmp_eq_u64 vcc, exec
	s_cbranch_scc1 .Lring_norare_a0
	s_nop 15
	s_nop 15
	v_max3_f32 v240, v173, v177, v165
	v_max3_f32 v240, v240, v166, v174
	v_max3_f32 v240, v240, v178, v167
	v_max3_f32 v240, v240, v168, v175
	v_max3_f32 v240, v240, v179, v169
	v_max3_f32 v240, v240, v170, v176
	v_max3_f32 v240, v240, v180, v171
	v_max3_f32 v240, v240, v172, v154
	v_max3_f32 v240, v240, v155, v130
	v_max3_f32 v240, v240, v131, v128
	v_max3_f32 v240, v240, v129, v126
	v_max3_f32 v240, v240, v127, v124
	v_max3_f32 v240, v240, v125, v160
	v_max3_f32 v240, v240, v161, v158
	v_max3_f32 v240, v240, v159, v156
	v_max_f32_e32 v240, v240, v157
	v_mov_b32_e32 v241, v240
	s_nop 1
	v_permlane32_swap_b32_e32 v240, v241
	v_max_f32_e32 v240, v240, v241
	v_log_f32_e32 v249, v240
	s_nop 0
	v_ceil_f32_e32 v249, v249
	v_max_f32_e32 v249, 0, v249
	v_exp_f32_e64 v252, -v249
	s_nop 0
	v_fmamk_f32 v153, v249, 0x41000000, v153
	v_mul_f32_e32 v173, v173, v252
	v_mul_f32_e32 v177, v177, v252
	v_mul_f32_e32 v165, v165, v252
	v_mul_f32_e32 v166, v166, v252
	v_mul_f32_e32 v174, v174, v252
	v_mul_f32_e32 v178, v178, v252
	v_mul_f32_e32 v167, v167, v252
	v_mul_f32_e32 v168, v168, v252
	v_mul_f32_e32 v175, v175, v252
	v_mul_f32_e32 v179, v179, v252
	v_mul_f32_e32 v169, v169, v252
	v_mul_f32_e32 v170, v170, v252
	v_mul_f32_e32 v176, v176, v252
	v_mul_f32_e32 v180, v180, v252
	v_mul_f32_e32 v171, v171, v252
	v_mul_f32_e32 v172, v172, v252
	v_mul_f32_e32 v154, v154, v252
	v_mul_f32_e32 v155, v155, v252
	v_mul_f32_e32 v130, v130, v252
	v_mul_f32_e32 v131, v131, v252
	v_mul_f32_e32 v128, v128, v252
	v_mul_f32_e32 v129, v129, v252
	v_mul_f32_e32 v126, v126, v252
	v_mul_f32_e32 v127, v127, v252
	v_mul_f32_e32 v124, v124, v252
	v_mul_f32_e32 v125, v125, v252
	v_mul_f32_e32 v160, v160, v252
	v_mul_f32_e32 v161, v161, v252
	v_mul_f32_e32 v158, v158, v252
	v_mul_f32_e32 v159, v159, v252
	v_mul_f32_e32 v156, v156, v252
	v_mul_f32_e32 v157, v157, v252
	v_mul_f32_e32 v162, v162, v252
	v_mul_f32_e32 v145, v145, v252
	v_sub_f32_e32 v84, v84, v249
	v_sub_f32_e32 v85, v85, v249
	v_sub_f32_e32 v86, v86, v249
	v_sub_f32_e32 v87, v87, v249
	v_sub_f32_e32 v88, v88, v249
	v_sub_f32_e32 v89, v89, v249
	v_sub_f32_e32 v90, v90, v249
	v_sub_f32_e32 v91, v91, v249
	v_sub_f32_e32 v92, v92, v249
	v_sub_f32_e32 v93, v93, v249
	v_sub_f32_e32 v94, v94, v249
	v_sub_f32_e32 v95, v95, v249
	v_sub_f32_e32 v96, v96, v249
	v_sub_f32_e32 v97, v97, v249
	v_sub_f32_e32 v98, v98, v249
	v_sub_f32_e32 v99, v99, v249
	v_sub_f32_e32 v68, v68, v249
	v_sub_f32_e32 v69, v69, v249
	v_sub_f32_e32 v70, v70, v249
	v_sub_f32_e32 v71, v71, v249
	v_sub_f32_e32 v72, v72, v249
	v_sub_f32_e32 v73, v73, v249
	v_sub_f32_e32 v74, v74, v249
	v_sub_f32_e32 v75, v75, v249
	v_sub_f32_e32 v76, v76, v249
	v_sub_f32_e32 v77, v77, v249
	v_sub_f32_e32 v78, v78, v249
	v_sub_f32_e32 v79, v79, v249
	v_sub_f32_e32 v80, v80, v249
	v_sub_f32_e32 v81, v81, v249
	v_sub_f32_e32 v82, v82, v249
	v_sub_f32_e32 v83, v83, v249
	v_sub_f32_e32 v216, v216, v249
	v_sub_f32_e32 v217, v217, v249
	v_sub_f32_e32 v218, v218, v249
	v_sub_f32_e32 v219, v219, v249
	v_sub_f32_e32 v220, v220, v249
	v_sub_f32_e32 v221, v221, v249
	v_sub_f32_e32 v222, v222, v249
	v_sub_f32_e32 v223, v223, v249
	v_sub_f32_e32 v224, v224, v249
	v_sub_f32_e32 v225, v225, v249
	v_sub_f32_e32 v226, v226, v249
	v_sub_f32_e32 v227, v227, v249
	v_sub_f32_e32 v228, v228, v249
	v_sub_f32_e32 v229, v229, v249
	v_sub_f32_e32 v230, v230, v249
	v_sub_f32_e32 v231, v231, v249
	s_and_saveexec_b64 s[8:9], s[6:7]
	ds_write_b32 v184, v252 offset:128
	s_or_b64 exec, exec, s[8:9]
	s_waitcnt lgkmcnt(0)
	v_add_u32_e32 v253, v135, v185
	ds_read_b128 v[212:215], v253 offset:224
	ds_read_b128 v[208:211], v253 offset:192
	ds_read_b128 v[204:207], v253 offset:160
	ds_read_b128 v[200:203], v253 offset:128
	s_waitcnt lgkmcnt(0)
	v_pk_mul_f32 v[52:53], v[52:53], v[200:201]
	v_pk_mul_f32 v[54:55], v[54:55], v[202:203]
	v_pk_mul_f32 v[56:57], v[56:57], v[204:205]
	v_pk_mul_f32 v[58:59], v[58:59], v[206:207]
	v_pk_mul_f32 v[60:61], v[60:61], v[208:209]
	v_pk_mul_f32 v[62:63], v[62:63], v[210:211]
	v_pk_mul_f32 v[64:65], v[64:65], v[212:213]
	v_pk_mul_f32 v[66:67], v[66:67], v[214:215]
	v_pk_mul_f32 v[36:37], v[36:37], v[200:201]
	v_pk_mul_f32 v[38:39], v[38:39], v[202:203]
	v_pk_mul_f32 v[40:41], v[40:41], v[204:205]
	v_pk_mul_f32 v[42:43], v[42:43], v[206:207]
	v_pk_mul_f32 v[44:45], v[44:45], v[208:209]
	v_pk_mul_f32 v[46:47], v[46:47], v[210:211]
	v_pk_mul_f32 v[48:49], v[48:49], v[212:213]
	v_pk_mul_f32 v[50:51], v[50:51], v[214:215]
	v_pk_mul_f32 v[20:21], v[20:21], v[200:201]
	v_pk_mul_f32 v[22:23], v[22:23], v[202:203]
	v_pk_mul_f32 v[24:25], v[24:25], v[204:205]
	v_pk_mul_f32 v[26:27], v[26:27], v[206:207]
	v_pk_mul_f32 v[28:29], v[28:29], v[208:209]
	v_pk_mul_f32 v[30:31], v[30:31], v[210:211]
	v_pk_mul_f32 v[32:33], v[32:33], v[212:213]
	v_pk_mul_f32 v[34:35], v[34:35], v[214:215]
	v_pk_mul_f32 v[4:5], v[4:5], v[200:201]
	v_pk_mul_f32 v[6:7], v[6:7], v[202:203]
	v_pk_mul_f32 v[8:9], v[8:9], v[204:205]
	v_pk_mul_f32 v[10:11], v[10:11], v[206:207]
	v_pk_mul_f32 v[12:13], v[12:13], v[208:209]
	v_pk_mul_f32 v[14:15], v[14:15], v[210:211]
	v_pk_mul_f32 v[16:17], v[16:17], v[212:213]
	v_pk_mul_f32 v[18:19], v[18:19], v[214:215]
	v_cvt_pk_fp8_f32 v232, v173, v177
	v_cvt_pk_fp8_f32 v233, v174, v178
	v_cvt_pk_fp8_f32 v234, v175, v179
	v_cvt_pk_fp8_f32 v235, v176, v180
	v_cvt_pk_fp8_f32 v232, v165, v166 op_sel:[0,0,1]
	v_cvt_pk_fp8_f32 v233, v167, v168 op_sel:[0,0,1]
	v_cvt_pk_fp8_f32 v234, v169, v170 op_sel:[0,0,1]
	v_cvt_pk_fp8_f32 v235, v171, v172 op_sel:[0,0,1]
	v_cvt_pk_fp8_f32 v236, v154, v155
	v_cvt_pk_fp8_f32 v237, v128, v129
	v_cvt_pk_fp8_f32 v238, v124, v125
	v_cvt_pk_fp8_f32 v239, v158, v159
	v_cvt_pk_fp8_f32 v236, v130, v131 op_sel:[0,0,1]
	v_cvt_pk_fp8_f32 v237, v126, v127 op_sel:[0,0,1]
	v_cvt_pk_fp8_f32 v238, v160, v161 op_sel:[0,0,1]
	v_cvt_pk_fp8_f32 v239, v156, v157 op_sel:[0,0,1]
	ds_read_b128 v[208:211], v197 offset:2048
	ds_read_b128 v[212:215], v198 offset:2048
.Lring_norare_a0:
	ds_read_b128 v[200:203], v197
	ds_read_b128 v[204:207], v198
	global_load_dwordx4 v[124:127], v[150:151], off offset:-64
	v_add_u32_e32 v252, 0xffffe000, v152
	v_mov_b32_e32 v253, v3
	v_lshl_add_u64 v[252:253], v[148:149], 0, v[252:253]
	global_load_dwordx4 v[128:131], v[252:253], off
	v_add_f32_e32 v145, v145, v162
	v_exp_f32_e32 v165, v84
	v_exp_f32_e32 v169, v85
	v_exp_f32_e32 v2, v86
	s_waitcnt lgkmcnt(2)
	v_mfma_scale_f32_32x32x64_f8f6f4 v[36:51], v[232:239], v[208:215], v[36:51], v188, v188 op_sel_hi:[0,0,0]
	ds_read_b128 v[208:211], v197 offset:6144
	ds_read_b128 v[212:215], v198 offset:6144
	v_exp_f32_e32 v155, v87
	v_exp_f32_e32 v166, v88
	v_exp_f32_e32 v170, v89
	v_exp_f32_e32 v156, v90
	v_exp_f32_e32 v157, v91
	v_exp_f32_e32 v167, v92
	v_exp_f32_e32 v171, v93
	s_waitcnt lgkmcnt(2)
	v_mfma_scale_f32_32x32x64_f8f6f4 v[52:67], v[232:239], v[200:207], v[52:67], v188, v188 op_sel_hi:[0,0,0]
	ds_read_b128 v[200:203], v197 offset:4096
	ds_read_b128 v[204:207], v198 offset:4096
	v_exp_f32_e32 v158, v94
	v_exp_f32_e32 v159, v95
	v_exp_f32_e32 v168, v96
	v_exp_f32_e32 v172, v97
	v_exp_f32_e32 v160, v98
	v_exp_f32_e32 v161, v99
	v_exp_f32_e32 v173, v68
	s_waitcnt lgkmcnt(2)
	v_mfma_scale_f32_32x32x64_f8f6f4 v[4:19], v[232:239], v[208:215], v[4:19], v188, v188 op_sel_hi:[0,0,0]
	v_exp_f32_e32 v174, v69
	v_exp_f32_e32 v175, v70
	v_exp_f32_e32 v176, v71
	v_exp_f32_e32 v177, v72
	v_exp_f32_e32 v178, v73
	v_exp_f32_e32 v179, v74
	v_exp_f32_e32 v180, v75
	v_exp_f32_e32 v181, v76
	s_waitcnt lgkmcnt(0)
	v_mfma_scale_f32_32x32x64_f8f6f4 v[20:35], v[232:239], v[200:207], v[20:35], v188, v188 op_sel_hi:[0,0,0]
	v_exp_f32_e32 v182, v77
	v_exp_f32_e32 v183, v78
	v_exp_f32_e32 v246, v79
	v_exp_f32_e32 v248, v80
	v_exp_f32_e32 v250, v81
	v_exp_f32_e32 v251, v82
	v_exp_f32_e32 v164, v83
	s_waitcnt lgkmcnt(0)
	s_barrier
	s_waitcnt vmcnt(0)
	s_cmp_gt_u32 s15, 60
	s_cselect_b64 s[8:9], -1, 0
	s_and_b64 vcc, exec, s[8:9]
	s_cbranch_vccnz .Lring_noload_b0
	v_mov_b32_e32 v252, v152
	v_mov_b32_e32 v253, v3
	v_lshl_add_u64 v[120:121], v[148:149], 0, v[252:253]
	global_load_dwordx4 v[116:119], v[150:151], off
	s_nop 0
	global_load_dwordx4 v[120:123], v[120:121], off
.Lring_noload_b0:
	ds_read_b128 v[68:71], v192 offset:40960
	ds_read_b128 v[72:75], v193 offset:40960
	ds_read_b128 v[208:211], v194 offset:40960
	ds_read_b128 v[212:215], v195 offset:40960
	ds_read_b128 v[200:203], v192 offset:45056
	ds_read_b128 v[204:207], v193 offset:45056
	v_mov_b32_e32 v254, v124
	v_mov_b32_e32 v255, v126
	ds_write_b64 v189, v[254:255] offset:24576
	v_mov_b32_e32 v244, v125
	v_mov_b32_e32 v245, v127
	ds_write_b64 v190, v[244:245] offset:24576
	ds_write_b128 v191, v[128:131] offset:57344
	v_cvt_pk_fp8_f32 v232, v165, v169
	v_cvt_pk_fp8_f32 v233, v166, v170
	v_cvt_pk_fp8_f32 v234, v167, v171
	v_cvt_pk_fp8_f32 v235, v168, v172
	v_cvt_pk_fp8_f32 v232, v2, v155 op_sel:[0,0,1]
	v_cvt_pk_fp8_f32 v233, v156, v157 op_sel:[0,0,1]
	v_cvt_pk_fp8_f32 v234, v158, v159 op_sel:[0,0,1]
	s_waitcnt lgkmcnt(7)
	v_mfma_scale_f32_32x32x64_f8f6f4 v[84:99], v[68:75], v[100:107], v[216:231], v188, v247 op_sel_hi:[0,0,0]
	v_cvt_pk_fp8_f32 v235, v160, v161 op_sel:[0,0,1]
	v_cvt_pk_fp8_f32 v236, v173, v174
	v_cvt_pk_fp8_f32 v237, v177, v178
	v_cvt_pk_fp8_f32 v238, v181, v182
	v_cvt_pk_fp8_f32 v239, v248, v250
	v_cvt_pk_fp8_f32 v236, v175, v176 op_sel:[0,0,1]
	v_cvt_pk_fp8_f32 v237, v179, v180 op_sel:[0,0,1]
	v_cvt_pk_fp8_f32 v238, v183, v246 op_sel:[0,0,1]
	v_cvt_pk_fp8_f32 v239, v251, v164 op_sel:[0,0,1]
	v_add_f32_e32 v241, v173, v174
	v_add_f32_e32 v240, v165, v169
	s_waitcnt lgkmcnt(5)
	v_mfma_scale_f32_32x32x64_f8f6f4 v[84:99], v[208:215], v[108:115], v[84:99], v188, v247 op_sel_hi:[0,0,0]
	ds_read_b128 v[208:211], v197 offset:18432
	ds_read_b128 v[212:215], v198 offset:18432
	v_add_f32_e32 v241, v175, v241
	v_add_f32_e32 v240, v2, v240
	v_add_f32_e32 v241, v176, v241
	v_add_f32_e32 v240, v155, v240
	v_add_f32_e32 v241, v177, v241
	v_add_f32_e32 v240, v166, v240
	v_add_f32_e32 v241, v178, v241
	v_add_f32_e32 v240, v170, v240
	v_add_f32_e32 v241, v179, v241
	v_add_f32_e32 v240, v156, v240
	v_add_f32_e32 v241, v180, v241
	s_waitcnt lgkmcnt(5)
	v_mfma_scale_f32_32x32x64_f8f6f4 v[68:83], v[200:207], v[100:107], v[216:231], v188, v247 op_sel_hi:[0,0,0]
	ds_read_b128 v[200:203], v194 offset:45056
	ds_read_b128 v[204:207], v195 offset:45056
	v_add_f32_e32 v240, v157, v240
	v_add_f32_e32 v241, v181, v241
	v_add_f32_e32 v240, v167, v240
	v_add_f32_e32 v241, v182, v241
	v_add_f32_e32 v240, v171, v240
	v_add_f32_e32 v241, v183, v241
	v_add_f32_e32 v240, v158, v240
	v_add_f32_e32 v241, v246, v241
	v_add_f32_e32 v240, v159, v240
	v_add_f32_e32 v241, v248, v241
	v_add_f32_e32 v240, v168, v240
	v_add_f32_e32 v241, v250, v241
	s_waitcnt lgkmcnt(0)
	v_mfma_scale_f32_32x32x64_f8f6f4 v[68:83], v[200:207], v[108:115], v[68:83], v188, v247 op_sel_hi:[0,0,0]
	v_add_f32_e32 v240, v172, v240
	v_add_f32_e32 v241, v251, v241
	v_add_f32_e32 v240, v160, v240
	v_add_f32_e32 v241, v164, v241
	v_add_f32_e32 v240, v161, v240
	v_add_f32_e32 v162, v240, v241
	v_mov_b32_e32 v163, v162
	s_nop 0
	s_nop 0
	v_permlane32_swap_b32_e32 v162, v163
	v_add_f32_e32 v162, v162, v163
	v_cmp_ge_f32_e32 vcc, 0x43c80000, v162
	s_cmp_eq_u64 vcc, exec
	s_cbranch_scc1 .Lring_norare_b0
	s_nop 15
	s_nop 15
	v_max3_f32 v240, v165, v169, v2
	v_max3_f32 v240, v240, v155, v166
	v_max3_f32 v240, v240, v170, v156
	v_max3_f32 v240, v240, v157, v167
	v_max3_f32 v240, v240, v171, v158
	v_max3_f32 v240, v240, v159, v168
	v_max3_f32 v240, v240, v172, v160
	v_max3_f32 v240, v240, v161, v173
	v_max3_f32 v240, v240, v174, v175
	v_max3_f32 v240, v240, v176, v177
	v_max3_f32 v240, v240, v178, v179
	v_max3_f32 v240, v240, v180, v181
	v_max3_f32 v240, v240, v182, v183
	v_max3_f32 v240, v240, v246, v248
	v_max3_f32 v240, v240, v250, v251
	v_max_f32_e32 v240, v240, v164
	v_mov_b32_e32 v241, v240
	s_nop 1
	v_permlane32_swap_b32_e32 v240, v241
	v_max_f32_e32 v240, v240, v241
	v_log_f32_e32 v249, v240
	s_nop 0
	v_ceil_f32_e32 v249, v249
	v_max_f32_e32 v249, 0, v249
	v_exp_f32_e64 v252, -v249
	s_nop 0
	v_fmamk_f32 v153, v249, 0x41000000, v153
	v_mul_f32_e32 v165, v165, v252
	v_mul_f32_e32 v169, v169, v252
	v_mul_f32_e32 v2, v2, v252
	v_mul_f32_e32 v155, v155, v252
	v_mul_f32_e32 v166, v166, v252
	v_mul_f32_e32 v170, v170, v252
	v_mul_f32_e32 v156, v156, v252
	v_mul_f32_e32 v157, v157, v252
	v_mul_f32_e32 v167, v167, v252
	v_mul_f32_e32 v171, v171, v252
	v_mul_f32_e32 v158, v158, v252
	v_mul_f32_e32 v159, v159, v252
	v_mul_f32_e32 v168, v168, v252
	v_mul_f32_e32 v172, v172, v252
	v_mul_f32_e32 v160, v160, v252
	v_mul_f32_e32 v161, v161, v252
	v_mul_f32_e32 v173, v173, v252
	v_mul_f32_e32 v174, v174, v252
	v_mul_f32_e32 v175, v175, v252
	v_mul_f32_e32 v176, v176, v252
	v_mul_f32_e32 v177, v177, v252
	v_mul_f32_e32 v178, v178, v252
	v_mul_f32_e32 v179, v179, v252
	v_mul_f32_e32 v180, v180, v252
	v_mul_f32_e32 v181, v181, v252
	v_mul_f32_e32 v182, v182, v252
	v_mul_f32_e32 v183, v183, v252
	v_mul_f32_e32 v246, v246, v252
	v_mul_f32_e32 v248, v248, v252
	v_mul_f32_e32 v250, v250, v252
	v_mul_f32_e32 v251, v251, v252
	v_mul_f32_e32 v164, v164, v252
	v_mul_f32_e32 v162, v162, v252
	v_mul_f32_e32 v145, v145, v252
	v_sub_f32_e32 v84, v84, v249
	v_sub_f32_e32 v85, v85, v249
	v_sub_f32_e32 v86, v86, v249
	v_sub_f32_e32 v87, v87, v249
	v_sub_f32_e32 v88, v88, v249
	v_sub_f32_e32 v89, v89, v249
	v_sub_f32_e32 v90, v90, v249
	v_sub_f32_e32 v91, v91, v249
	v_sub_f32_e32 v92, v92, v249
	v_sub_f32_e32 v93, v93, v249
	v_sub_f32_e32 v94, v94, v249
	v_sub_f32_e32 v95, v95, v249
	v_sub_f32_e32 v96, v96, v249
	v_sub_f32_e32 v97, v97, v249
	v_sub_f32_e32 v98, v98, v249
	v_sub_f32_e32 v99, v99, v249
	v_sub_f32_e32 v68, v68, v249
	v_sub_f32_e32 v69, v69, v249
	v_sub_f32_e32 v70, v70, v249
	v_sub_f32_e32 v71, v71, v249
	v_sub_f32_e32 v72, v72, v249
	v_sub_f32_e32 v73, v73, v249
	v_sub_f32_e32 v74, v74, v249
	v_sub_f32_e32 v75, v75, v249
	v_sub_f32_e32 v76, v76, v249
	v_sub_f32_e32 v77, v77, v249
	v_sub_f32_e32 v78, v78, v249
	v_sub_f32_e32 v79, v79, v249
	v_sub_f32_e32 v80, v80, v249
	v_sub_f32_e32 v81, v81, v249
	v_sub_f32_e32 v82, v82, v249
	v_sub_f32_e32 v83, v83, v249
	v_sub_f32_e32 v216, v216, v249
	v_sub_f32_e32 v217, v217, v249
	v_sub_f32_e32 v218, v218, v249
	v_sub_f32_e32 v219, v219, v249
	v_sub_f32_e32 v220, v220, v249
	v_sub_f32_e32 v221, v221, v249
	v_sub_f32_e32 v222, v222, v249
	v_sub_f32_e32 v223, v223, v249
	v_sub_f32_e32 v224, v224, v249
	v_sub_f32_e32 v225, v225, v249
	v_sub_f32_e32 v226, v226, v249
	v_sub_f32_e32 v227, v227, v249
	v_sub_f32_e32 v228, v228, v249
	v_sub_f32_e32 v229, v229, v249
	v_sub_f32_e32 v230, v230, v249
	v_sub_f32_e32 v231, v231, v249
	s_and_saveexec_b64 s[10:11], s[6:7]
	ds_write_b32 v184, v252 offset:128
	s_or_b64 exec, exec, s[10:11]
	s_waitcnt lgkmcnt(0)
	v_add_u32_e32 v253, v135, v185
	ds_read_b128 v[212:215], v253 offset:224
	ds_read_b128 v[208:211], v253 offset:192
	ds_read_b128 v[204:207], v253 offset:160
	ds_read_b128 v[200:203], v253 offset:128
	s_waitcnt lgkmcnt(0)
	v_pk_mul_f32 v[52:53], v[52:53], v[200:201]
	v_pk_mul_f32 v[54:55], v[54:55], v[202:203]
	v_pk_mul_f32 v[56:57], v[56:57], v[204:205]
	v_pk_mul_f32 v[58:59], v[58:59], v[206:207]
	v_pk_mul_f32 v[60:61], v[60:61], v[208:209]
	v_pk_mul_f32 v[62:63], v[62:63], v[210:211]
	v_pk_mul_f32 v[64:65], v[64:65], v[212:213]
	v_pk_mul_f32 v[66:67], v[66:67], v[214:215]
	v_pk_mul_f32 v[36:37], v[36:37], v[200:201]
	v_pk_mul_f32 v[38:39], v[38:39], v[202:203]
	v_pk_mul_f32 v[40:41], v[40:41], v[204:205]
	v_pk_mul_f32 v[42:43], v[42:43], v[206:207]
	v_pk_mul_f32 v[44:45], v[44:45], v[208:209]
	v_pk_mul_f32 v[46:47], v[46:47], v[210:211]
	v_pk_mul_f32 v[48:49], v[48:49], v[212:213]
	v_pk_mul_f32 v[50:51], v[50:51], v[214:215]
	v_pk_mul_f32 v[20:21], v[20:21], v[200:201]
	v_pk_mul_f32 v[22:23], v[22:23], v[202:203]
	v_pk_mul_f32 v[24:25], v[24:25], v[204:205]
	v_pk_mul_f32 v[26:27], v[26:27], v[206:207]
	v_pk_mul_f32 v[28:29], v[28:29], v[208:209]
	v_pk_mul_f32 v[30:31], v[30:31], v[210:211]
	v_pk_mul_f32 v[32:33], v[32:33], v[212:213]
	v_pk_mul_f32 v[34:35], v[34:35], v[214:215]
	v_pk_mul_f32 v[4:5], v[4:5], v[200:201]
	v_pk_mul_f32 v[6:7], v[6:7], v[202:203]
	v_pk_mul_f32 v[8:9], v[8:9], v[204:205]
	v_pk_mul_f32 v[10:11], v[10:11], v[206:207]
	v_pk_mul_f32 v[12:13], v[12:13], v[208:209]
	v_pk_mul_f32 v[14:15], v[14:15], v[210:211]
	v_pk_mul_f32 v[16:17], v[16:17], v[212:213]
	v_pk_mul_f32 v[18:19], v[18:19], v[214:215]
	v_cvt_pk_fp8_f32 v232, v165, v169
	v_cvt_pk_fp8_f32 v233, v166, v170
	v_cvt_pk_fp8_f32 v234, v167, v171
	v_cvt_pk_fp8_f32 v235, v168, v172
	v_cvt_pk_fp8_f32 v232, v2, v155 op_sel:[0,0,1]
	v_cvt_pk_fp8_f32 v233, v156, v157 op_sel:[0,0,1]
	v_cvt_pk_fp8_f32 v234, v158, v159 op_sel:[0,0,1]
	v_cvt_pk_fp8_f32 v235, v160, v161 op_sel:[0,0,1]
	v_cvt_pk_fp8_f32 v236, v173, v174
	v_cvt_pk_fp8_f32 v237, v177, v178
	v_cvt_pk_fp8_f32 v238, v181, v182
	v_cvt_pk_fp8_f32 v239, v248, v250
	v_cvt_pk_fp8_f32 v236, v175, v176 op_sel:[0,0,1]
	v_cvt_pk_fp8_f32 v237, v179, v180 op_sel:[0,0,1]
	v_cvt_pk_fp8_f32 v238, v183, v246 op_sel:[0,0,1]
	v_cvt_pk_fp8_f32 v239, v251, v164 op_sel:[0,0,1]
	ds_read_b128 v[208:211], v197 offset:18432
	ds_read_b128 v[212:215], v198 offset:18432
.Lring_norare_b0:
	ds_read_b128 v[200:203], v197 offset:16384
	ds_read_b128 v[204:207], v198 offset:16384
	v_add_f32_e32 v145, v145, v162
	v_exp_f32_e32 v173, v84
	v_exp_f32_e32 v177, v85
	v_exp_f32_e32 v165, v86
	v_exp_f32_e32 v166, v87
	v_exp_f32_e32 v174, v88
	s_waitcnt lgkmcnt(2)
	v_mfma_scale_f32_32x32x64_f8f6f4 v[36:51], v[232:239], v[208:215], v[36:51], v188, v188 op_sel_hi:[0,0,0]
	ds_read_b128 v[208:211], v197 offset:22528
	ds_read_b128 v[212:215], v198 offset:22528
	v_exp_f32_e32 v178, v89
	v_exp_f32_e32 v167, v90
	v_exp_f32_e32 v168, v91
	v_exp_f32_e32 v175, v92
	v_exp_f32_e32 v179, v93
	v_exp_f32_e32 v169, v94
	v_exp_f32_e32 v170, v95
	s_waitcnt lgkmcnt(2)
	v_mfma_scale_f32_32x32x64_f8f6f4 v[52:67], v[232:239], v[200:207], v[52:67], v188, v188 op_sel_hi:[0,0,0]
	ds_read_b128 v[200:203], v197 offset:20480
	ds_read_b128 v[204:207], v198 offset:20480
	v_exp_f32_e32 v176, v96
	v_exp_f32_e32 v180, v97
	v_exp_f32_e32 v171, v98
	v_exp_f32_e32 v172, v99
	v_exp_f32_e32 v154, v68
	v_exp_f32_e32 v155, v69
	v_exp_f32_e32 v130, v70
	s_waitcnt lgkmcnt(2)
	v_mfma_scale_f32_32x32x64_f8f6f4 v[4:19], v[232:239], v[208:215], v[4:19], v188, v188 op_sel_hi:[0,0,0]
	v_exp_f32_e32 v131, v71
	v_exp_f32_e32 v128, v72
	v_exp_f32_e32 v129, v73
	v_exp_f32_e32 v126, v74
	v_exp_f32_e32 v127, v75
	v_exp_f32_e32 v124, v76
	v_exp_f32_e32 v125, v77
	s_waitcnt lgkmcnt(0)
	v_mfma_scale_f32_32x32x64_f8f6f4 v[20:35], v[232:239], v[200:207], v[20:35], v188, v188 op_sel_hi:[0,0,0]
	v_exp_f32_e32 v160, v78
	v_exp_f32_e32 v161, v79
	v_exp_f32_e32 v158, v80
	v_exp_f32_e32 v159, v81
	v_exp_f32_e32 v156, v82
	v_exp_f32_e32 v157, v83
	s_add_i32 s15, s15, 2
	v_lshl_add_u64 v[150:151], v[150:151], 0, s[28:29]
	v_add_u32_e32 v152, 0x4000, v152
	s_and_b64 vcc, exec, s[8:9]
	s_waitcnt lgkmcnt(0)
	s_barrier
	s_cbranch_vccnz .LBB0_421
	s_waitcnt vmcnt(0)
	ds_read_b128 v[68:71], v192 offset:57344
	ds_read_b128 v[72:75], v193 offset:57344
	ds_read_b128 v[208:211], v194 offset:57344
	ds_read_b128 v[212:215], v195 offset:57344
	ds_read_b128 v[200:203], v192 offset:61440
	ds_read_b128 v[204:207], v193 offset:61440
	v_mov_b32_e32 v254, v116
	v_mov_b32_e32 v255, v118
	ds_write_b64 v189, v[254:255]
	v_mov_b32_e32 v244, v117
	v_mov_b32_e32 v245, v119
	ds_write_b64 v190, v[244:245]
	ds_write_b128 v191, v[120:123] offset:32768
	v_cvt_pk_fp8_f32 v232, v173, v177
	v_cvt_pk_fp8_f32 v233, v174, v178
	v_cvt_pk_fp8_f32 v234, v175, v179
	v_cvt_pk_fp8_f32 v235, v176, v180
	v_cvt_pk_fp8_f32 v232, v165, v166 op_sel:[0,0,1]
	v_cvt_pk_fp8_f32 v233, v167, v168 op_sel:[0,0,1]
	v_cvt_pk_fp8_f32 v234, v169, v170 op_sel:[0,0,1]
	s_waitcnt lgkmcnt(7)
	v_mfma_scale_f32_32x32x64_f8f6f4 v[84:99], v[68:75], v[100:107], v[216:231], v188, v247 op_sel_hi:[0,0,0]
	v_cvt_pk_fp8_f32 v235, v171, v172 op_sel:[0,0,1]
	v_cvt_pk_fp8_f32 v236, v154, v155
	v_cvt_pk_fp8_f32 v237, v128, v129
	v_cvt_pk_fp8_f32 v238, v124, v125
	v_cvt_pk_fp8_f32 v239, v158, v159
	v_cvt_pk_fp8_f32 v236, v130, v131 op_sel:[0,0,1]
	v_cvt_pk_fp8_f32 v237, v126, v127 op_sel:[0,0,1]
	v_cvt_pk_fp8_f32 v238, v160, v161 op_sel:[0,0,1]
	v_cvt_pk_fp8_f32 v239, v156, v157 op_sel:[0,0,1]
	v_add_f32_e32 v241, v154, v155
	v_add_f32_e32 v240, v173, v177
	s_waitcnt lgkmcnt(5)
	v_mfma_scale_f32_32x32x64_f8f6f4 v[84:99], v[208:215], v[108:115], v[84:99], v188, v247 op_sel_hi:[0,0,0]
	ds_read_b128 v[208:211], v197 offset:10240
	ds_read_b128 v[212:215], v198 offset:10240
	v_add_f32_e32 v241, v130, v241
	v_add_f32_e32 v240, v165, v240
	v_add_f32_e32 v241, v131, v241
	v_add_f32_e32 v240, v166, v240
	v_add_f32_e32 v241, v128, v241
	v_add_f32_e32 v240, v174, v240
	v_add_f32_e32 v241, v129, v241
	v_add_f32_e32 v240, v178, v240
	v_add_f32_e32 v241, v126, v241
	v_add_f32_e32 v240, v167, v240
	v_add_f32_e32 v241, v127, v241
	s_waitcnt lgkmcnt(5)
	v_mfma_scale_f32_32x32x64_f8f6f4 v[68:83], v[200:207], v[100:107], v[216:231], v188, v247 op_sel_hi:[0,0,0]
	ds_read_b128 v[200:203], v194 offset:61440
	ds_read_b128 v[204:207], v195 offset:61440
	v_add_f32_e32 v240, v168, v240
	v_add_f32_e32 v241, v124, v241
	v_add_f32_e32 v240, v175, v240
	v_add_f32_e32 v241, v125, v241
	v_add_f32_e32 v240, v179, v240
	v_add_f32_e32 v241, v160, v241
	v_add_f32_e32 v240, v169, v240
	v_add_f32_e32 v241, v161, v241
	v_add_f32_e32 v240, v170, v240
	v_add_f32_e32 v241, v158, v241
	v_add_f32_e32 v240, v176, v240
	v_add_f32_e32 v241, v159, v241
	s_waitcnt lgkmcnt(0)
	v_mfma_scale_f32_32x32x64_f8f6f4 v[68:83], v[200:207], v[108:115], v[68:83], v188, v247 op_sel_hi:[0,0,0]
	v_add_f32_e32 v240, v180, v240
	v_add_f32_e32 v241, v156, v241
	v_add_f32_e32 v240, v171, v240
	v_add_f32_e32 v241, v157, v241
	v_add_f32_e32 v240, v172, v240
	v_add_f32_e32 v162, v240, v241
	v_mov_b32_e32 v163, v162
	s_nop 0
	s_nop 0
	v_permlane32_swap_b32_e32 v162, v163
	v_add_f32_e32 v162, v162, v163
	v_cmp_ge_f32_e32 vcc, 0x43c80000, v162
	s_cmp_eq_u64 vcc, exec
	s_cbranch_scc1 .Lring_norare_a1
	s_nop 15
	s_nop 15
	v_max3_f32 v240, v173, v177, v165
	v_max3_f32 v240, v240, v166, v174
	v_max3_f32 v240, v240, v178, v167
	v_max3_f32 v240, v240, v168, v175
	v_max3_f32 v240, v240, v179, v169
	v_max3_f32 v240, v240, v170, v176
	v_max3_f32 v240, v240, v180, v171
	v_max3_f32 v240, v240, v172, v154
	v_max3_f32 v240, v240, v155, v130
	v_max3_f32 v240, v240, v131, v128
	v_max3_f32 v240, v240, v129, v126
	v_max3_f32 v240, v240, v127, v124
	v_max3_f32 v240, v240, v125, v160
	v_max3_f32 v240, v240, v161, v158
	v_max3_f32 v240, v240, v159, v156
	v_max_f32_e32 v240, v240, v157
	v_mov_b32_e32 v241, v240
	s_nop 1
	v_permlane32_swap_b32_e32 v240, v241
	v_max_f32_e32 v240, v240, v241
	v_log_f32_e32 v249, v240
	s_nop 0
	v_ceil_f32_e32 v249, v249
	v_max_f32_e32 v249, 0, v249
	v_exp_f32_e64 v252, -v249
	s_nop 0
	v_fmamk_f32 v153, v249, 0x41000000, v153
	v_mul_f32_e32 v173, v173, v252
	v_mul_f32_e32 v177, v177, v252
	v_mul_f32_e32 v165, v165, v252
	v_mul_f32_e32 v166, v166, v252
	v_mul_f32_e32 v174, v174, v252
	v_mul_f32_e32 v178, v178, v252
	v_mul_f32_e32 v167, v167, v252
	v_mul_f32_e32 v168, v168, v252
	v_mul_f32_e32 v175, v175, v252
	v_mul_f32_e32 v179, v179, v252
	v_mul_f32_e32 v169, v169, v252
	v_mul_f32_e32 v170, v170, v252
	v_mul_f32_e32 v176, v176, v252
	v_mul_f32_e32 v180, v180, v252
	v_mul_f32_e32 v171, v171, v252
	v_mul_f32_e32 v172, v172, v252
	v_mul_f32_e32 v154, v154, v252
	v_mul_f32_e32 v155, v155, v252
	v_mul_f32_e32 v130, v130, v252
	v_mul_f32_e32 v131, v131, v252
	v_mul_f32_e32 v128, v128, v252
	v_mul_f32_e32 v129, v129, v252
	v_mul_f32_e32 v126, v126, v252
	v_mul_f32_e32 v127, v127, v252
	v_mul_f32_e32 v124, v124, v252
	v_mul_f32_e32 v125, v125, v252
	v_mul_f32_e32 v160, v160, v252
	v_mul_f32_e32 v161, v161, v252
	v_mul_f32_e32 v158, v158, v252
	v_mul_f32_e32 v159, v159, v252
	v_mul_f32_e32 v156, v156, v252
	v_mul_f32_e32 v157, v157, v252
	v_mul_f32_e32 v162, v162, v252
	v_mul_f32_e32 v145, v145, v252
	v_sub_f32_e32 v84, v84, v249
	v_sub_f32_e32 v85, v85, v249
	v_sub_f32_e32 v86, v86, v249
	v_sub_f32_e32 v87, v87, v249
	v_sub_f32_e32 v88, v88, v249
	v_sub_f32_e32 v89, v89, v249
	v_sub_f32_e32 v90, v90, v249
	v_sub_f32_e32 v91, v91, v249
	v_sub_f32_e32 v92, v92, v249
	v_sub_f32_e32 v93, v93, v249
	v_sub_f32_e32 v94, v94, v249
	v_sub_f32_e32 v95, v95, v249
	v_sub_f32_e32 v96, v96, v249
	v_sub_f32_e32 v97, v97, v249
	v_sub_f32_e32 v98, v98, v249
	v_sub_f32_e32 v99, v99, v249
	v_sub_f32_e32 v68, v68, v249
	v_sub_f32_e32 v69, v69, v249
	v_sub_f32_e32 v70, v70, v249
	v_sub_f32_e32 v71, v71, v249
	v_sub_f32_e32 v72, v72, v249
	v_sub_f32_e32 v73, v73, v249
	v_sub_f32_e32 v74, v74, v249
	v_sub_f32_e32 v75, v75, v249
	v_sub_f32_e32 v76, v76, v249
	v_sub_f32_e32 v77, v77, v249
	v_sub_f32_e32 v78, v78, v249
	v_sub_f32_e32 v79, v79, v249
	v_sub_f32_e32 v80, v80, v249
	v_sub_f32_e32 v81, v81, v249
	v_sub_f32_e32 v82, v82, v249
	v_sub_f32_e32 v83, v83, v249
	v_sub_f32_e32 v216, v216, v249
	v_sub_f32_e32 v217, v217, v249
	v_sub_f32_e32 v218, v218, v249
	v_sub_f32_e32 v219, v219, v249
	v_sub_f32_e32 v220, v220, v249
	v_sub_f32_e32 v221, v221, v249
	v_sub_f32_e32 v222, v222, v249
	v_sub_f32_e32 v223, v223, v249
	v_sub_f32_e32 v224, v224, v249
	v_sub_f32_e32 v225, v225, v249
	v_sub_f32_e32 v226, v226, v249
	v_sub_f32_e32 v227, v227, v249
	v_sub_f32_e32 v228, v228, v249
	v_sub_f32_e32 v229, v229, v249
	v_sub_f32_e32 v230, v230, v249
	v_sub_f32_e32 v231, v231, v249
	s_and_saveexec_b64 s[8:9], s[6:7]
	ds_write_b32 v184, v252 offset:128
	s_or_b64 exec, exec, s[8:9]
	s_waitcnt lgkmcnt(0)
	v_add_u32_e32 v253, v135, v185
	ds_read_b128 v[212:215], v253 offset:224
	ds_read_b128 v[208:211], v253 offset:192
	ds_read_b128 v[204:207], v253 offset:160
	ds_read_b128 v[200:203], v253 offset:128
	s_waitcnt lgkmcnt(0)
	v_pk_mul_f32 v[52:53], v[52:53], v[200:201]
	v_pk_mul_f32 v[54:55], v[54:55], v[202:203]
	v_pk_mul_f32 v[56:57], v[56:57], v[204:205]
	v_pk_mul_f32 v[58:59], v[58:59], v[206:207]
	v_pk_mul_f32 v[60:61], v[60:61], v[208:209]
	v_pk_mul_f32 v[62:63], v[62:63], v[210:211]
	v_pk_mul_f32 v[64:65], v[64:65], v[212:213]
	v_pk_mul_f32 v[66:67], v[66:67], v[214:215]
	v_pk_mul_f32 v[36:37], v[36:37], v[200:201]
	v_pk_mul_f32 v[38:39], v[38:39], v[202:203]
	v_pk_mul_f32 v[40:41], v[40:41], v[204:205]
	v_pk_mul_f32 v[42:43], v[42:43], v[206:207]
	v_pk_mul_f32 v[44:45], v[44:45], v[208:209]
	v_pk_mul_f32 v[46:47], v[46:47], v[210:211]
	v_pk_mul_f32 v[48:49], v[48:49], v[212:213]
	v_pk_mul_f32 v[50:51], v[50:51], v[214:215]
	v_pk_mul_f32 v[20:21], v[20:21], v[200:201]
	v_pk_mul_f32 v[22:23], v[22:23], v[202:203]
	v_pk_mul_f32 v[24:25], v[24:25], v[204:205]
	v_pk_mul_f32 v[26:27], v[26:27], v[206:207]
	v_pk_mul_f32 v[28:29], v[28:29], v[208:209]
	v_pk_mul_f32 v[30:31], v[30:31], v[210:211]
	v_pk_mul_f32 v[32:33], v[32:33], v[212:213]
	v_pk_mul_f32 v[34:35], v[34:35], v[214:215]
	v_pk_mul_f32 v[4:5], v[4:5], v[200:201]
	v_pk_mul_f32 v[6:7], v[6:7], v[202:203]
	v_pk_mul_f32 v[8:9], v[8:9], v[204:205]
	v_pk_mul_f32 v[10:11], v[10:11], v[206:207]
	v_pk_mul_f32 v[12:13], v[12:13], v[208:209]
	v_pk_mul_f32 v[14:15], v[14:15], v[210:211]
	v_pk_mul_f32 v[16:17], v[16:17], v[212:213]
	v_pk_mul_f32 v[18:19], v[18:19], v[214:215]
	v_cvt_pk_fp8_f32 v232, v173, v177
	v_cvt_pk_fp8_f32 v233, v174, v178
	v_cvt_pk_fp8_f32 v234, v175, v179
	v_cvt_pk_fp8_f32 v235, v176, v180
	v_cvt_pk_fp8_f32 v232, v165, v166 op_sel:[0,0,1]
	v_cvt_pk_fp8_f32 v233, v167, v168 op_sel:[0,0,1]
	v_cvt_pk_fp8_f32 v234, v169, v170 op_sel:[0,0,1]
	v_cvt_pk_fp8_f32 v235, v171, v172 op_sel:[0,0,1]
	v_cvt_pk_fp8_f32 v236, v154, v155
	v_cvt_pk_fp8_f32 v237, v128, v129
	v_cvt_pk_fp8_f32 v238, v124, v125
	v_cvt_pk_fp8_f32 v239, v158, v159
	v_cvt_pk_fp8_f32 v236, v130, v131 op_sel:[0,0,1]
	v_cvt_pk_fp8_f32 v237, v126, v127 op_sel:[0,0,1]
	v_cvt_pk_fp8_f32 v238, v160, v161 op_sel:[0,0,1]
	v_cvt_pk_fp8_f32 v239, v156, v157 op_sel:[0,0,1]
	ds_read_b128 v[208:211], v197 offset:10240
	ds_read_b128 v[212:215], v198 offset:10240
.Lring_norare_a1:
	ds_read_b128 v[200:203], v197 offset:8192
	ds_read_b128 v[204:207], v198 offset:8192
	global_load_dwordx4 v[124:127], v[150:151], off offset:-64
	v_add_u32_e32 v252, 0xffffe000, v152
	v_mov_b32_e32 v253, v3
	v_lshl_add_u64 v[252:253], v[148:149], 0, v[252:253]
	global_load_dwordx4 v[128:131], v[252:253], off
	v_add_f32_e32 v145, v145, v162
	v_exp_f32_e32 v165, v84
	v_exp_f32_e32 v169, v85
	v_exp_f32_e32 v2, v86
	s_waitcnt lgkmcnt(2)
	v_mfma_scale_f32_32x32x64_f8f6f4 v[36:51], v[232:239], v[208:215], v[36:51], v188, v188 op_sel_hi:[0,0,0]
	ds_read_b128 v[208:211], v197 offset:14336
	ds_read_b128 v[212:215], v198 offset:14336
	v_exp_f32_e32 v155, v87
	v_exp_f32_e32 v166, v88
	v_exp_f32_e32 v170, v89
	v_exp_f32_e32 v156, v90
	v_exp_f32_e32 v157, v91
	v_exp_f32_e32 v167, v92
	v_exp_f32_e32 v171, v93
	s_waitcnt lgkmcnt(2)
	v_mfma_scale_f32_32x32x64_f8f6f4 v[52:67], v[232:239], v[200:207], v[52:67], v188, v188 op_sel_hi:[0,0,0]
	ds_read_b128 v[200:203], v197 offset:12288
	ds_read_b128 v[204:207], v198 offset:12288
	v_exp_f32_e32 v158, v94
	v_exp_f32_e32 v159, v95
	v_exp_f32_e32 v168, v96
	v_exp_f32_e32 v172, v97
	v_exp_f32_e32 v160, v98
	v_exp_f32_e32 v161, v99
	v_exp_f32_e32 v173, v68
	s_waitcnt lgkmcnt(2)
	v_mfma_scale_f32_32x32x64_f8f6f4 v[4:19], v[232:239], v[208:215], v[4:19], v188, v188 op_sel_hi:[0,0,0]
	v_exp_f32_e32 v174, v69
	v_exp_f32_e32 v175, v70
	v_exp_f32_e32 v176, v71
	v_exp_f32_e32 v177, v72
	v_exp_f32_e32 v178, v73
	v_exp_f32_e32 v179, v74
	v_exp_f32_e32 v180, v75
	v_exp_f32_e32 v181, v76
	s_waitcnt lgkmcnt(0)
	v_mfma_scale_f32_32x32x64_f8f6f4 v[20:35], v[232:239], v[200:207], v[20:35], v188, v188 op_sel_hi:[0,0,0]
	v_exp_f32_e32 v182, v77
	v_exp_f32_e32 v183, v78
	v_exp_f32_e32 v246, v79
	v_exp_f32_e32 v248, v80
	v_exp_f32_e32 v250, v81
	v_exp_f32_e32 v251, v82
	v_exp_f32_e32 v164, v83
	s_waitcnt lgkmcnt(0)
	s_barrier
	s_waitcnt vmcnt(0)
	s_cmp_gt_u32 s15, 60
	s_cselect_b64 s[8:9], -1, 0
	s_and_b64 vcc, exec, s[8:9]
	s_cbranch_vccnz .Lring_noload_b1
	v_mov_b32_e32 v252, v152
	v_mov_b32_e32 v253, v3
	v_lshl_add_u64 v[120:121], v[148:149], 0, v[252:253]
	global_load_dwordx4 v[116:119], v[150:151], off
	s_nop 0
	global_load_dwordx4 v[120:123], v[120:121], off
.Lring_noload_b1:
	ds_read_b128 v[68:71], v192 offset:32768
	ds_read_b128 v[72:75], v193 offset:32768
	ds_read_b128 v[208:211], v194 offset:32768
	ds_read_b128 v[212:215], v195 offset:32768
	ds_read_b128 v[200:203], v192 offset:36864
	ds_read_b128 v[204:207], v193 offset:36864
	v_mov_b32_e32 v254, v124
	v_mov_b32_e32 v255, v126
	ds_write_b64 v189, v[254:255] offset:16384
	v_mov_b32_e32 v244, v125
	v_mov_b32_e32 v245, v127
	ds_write_b64 v190, v[244:245] offset:16384
	ds_write_b128 v191, v[128:131] offset:49152
	v_cvt_pk_fp8_f32 v232, v165, v169
	v_cvt_pk_fp8_f32 v233, v166, v170
	v_cvt_pk_fp8_f32 v234, v167, v171
	v_cvt_pk_fp8_f32 v235, v168, v172
	v_cvt_pk_fp8_f32 v232, v2, v155 op_sel:[0,0,1]
	v_cvt_pk_fp8_f32 v233, v156, v157 op_sel:[0,0,1]
	v_cvt_pk_fp8_f32 v234, v158, v159 op_sel:[0,0,1]
	s_waitcnt lgkmcnt(7)
	v_mfma_scale_f32_32x32x64_f8f6f4 v[84:99], v[68:75], v[100:107], v[216:231], v188, v247 op_sel_hi:[0,0,0]
	v_cvt_pk_fp8_f32 v235, v160, v161 op_sel:[0,0,1]
	v_cvt_pk_fp8_f32 v236, v173, v174
	v_cvt_pk_fp8_f32 v237, v177, v178
	v_cvt_pk_fp8_f32 v238, v181, v182
	v_cvt_pk_fp8_f32 v239, v248, v250
	v_cvt_pk_fp8_f32 v236, v175, v176 op_sel:[0,0,1]
	v_cvt_pk_fp8_f32 v237, v179, v180 op_sel:[0,0,1]
	v_cvt_pk_fp8_f32 v238, v183, v246 op_sel:[0,0,1]
	v_cvt_pk_fp8_f32 v239, v251, v164 op_sel:[0,0,1]
	v_add_f32_e32 v241, v173, v174
	v_add_f32_e32 v240, v165, v169
	s_waitcnt lgkmcnt(5)
	v_mfma_scale_f32_32x32x64_f8f6f4 v[84:99], v[208:215], v[108:115], v[84:99], v188, v247 op_sel_hi:[0,0,0]
	ds_read_b128 v[208:211], v197 offset:26624
	ds_read_b128 v[212:215], v198 offset:26624
	v_add_f32_e32 v241, v175, v241
	v_add_f32_e32 v240, v2, v240
	v_add_f32_e32 v241, v176, v241
	v_add_f32_e32 v240, v155, v240
	v_add_f32_e32 v241, v177, v241
	v_add_f32_e32 v240, v166, v240
	v_add_f32_e32 v241, v178, v241
	v_add_f32_e32 v240, v170, v240
	v_add_f32_e32 v241, v179, v241
	v_add_f32_e32 v240, v156, v240
	v_add_f32_e32 v241, v180, v241
	s_waitcnt lgkmcnt(5)
	v_mfma_scale_f32_32x32x64_f8f6f4 v[68:83], v[200:207], v[100:107], v[216:231], v188, v247 op_sel_hi:[0,0,0]
	ds_read_b128 v[200:203], v194 offset:36864
	ds_read_b128 v[204:207], v195 offset:36864
	v_add_f32_e32 v240, v157, v240
	v_add_f32_e32 v241, v181, v241
	v_add_f32_e32 v240, v167, v240
	v_add_f32_e32 v241, v182, v241
	v_add_f32_e32 v240, v171, v240
	v_add_f32_e32 v241, v183, v241
	v_add_f32_e32 v240, v158, v240
	v_add_f32_e32 v241, v246, v241
	v_add_f32_e32 v240, v159, v240
	v_add_f32_e32 v241, v248, v241
	v_add_f32_e32 v240, v168, v240
	v_add_f32_e32 v241, v250, v241
	s_waitcnt lgkmcnt(0)
	v_mfma_scale_f32_32x32x64_f8f6f4 v[68:83], v[200:207], v[108:115], v[68:83], v188, v247 op_sel_hi:[0,0,0]
	v_add_f32_e32 v240, v172, v240
	v_add_f32_e32 v241, v251, v241
	v_add_f32_e32 v240, v160, v240
	v_add_f32_e32 v241, v164, v241
	v_add_f32_e32 v240, v161, v240
	v_add_f32_e32 v162, v240, v241
	v_mov_b32_e32 v163, v162
	s_nop 0
	s_nop 0
	v_permlane32_swap_b32_e32 v162, v163
	v_add_f32_e32 v162, v162, v163
	v_cmp_ge_f32_e32 vcc, 0x43c80000, v162
	s_cmp_eq_u64 vcc, exec
	s_cbranch_scc1 .Lring_norare_b1
	s_nop 15
	s_nop 15
	v_max3_f32 v240, v165, v169, v2
	v_max3_f32 v240, v240, v155, v166
	v_max3_f32 v240, v240, v170, v156
	v_max3_f32 v240, v240, v157, v167
	v_max3_f32 v240, v240, v171, v158
	v_max3_f32 v240, v240, v159, v168
	v_max3_f32 v240, v240, v172, v160
	v_max3_f32 v240, v240, v161, v173
	v_max3_f32 v240, v240, v174, v175
	v_max3_f32 v240, v240, v176, v177
	v_max3_f32 v240, v240, v178, v179
	v_max3_f32 v240, v240, v180, v181
	v_max3_f32 v240, v240, v182, v183
	v_max3_f32 v240, v240, v246, v248
	v_max3_f32 v240, v240, v250, v251
	v_max_f32_e32 v240, v240, v164
	v_mov_b32_e32 v241, v240
	s_nop 1
	v_permlane32_swap_b32_e32 v240, v241
	v_max_f32_e32 v240, v240, v241
	v_log_f32_e32 v249, v240
	s_nop 0
	v_ceil_f32_e32 v249, v249
	v_max_f32_e32 v249, 0, v249
	v_exp_f32_e64 v252, -v249
	s_nop 0
	v_fmamk_f32 v153, v249, 0x41000000, v153
	v_mul_f32_e32 v165, v165, v252
	v_mul_f32_e32 v169, v169, v252
	v_mul_f32_e32 v2, v2, v252
	v_mul_f32_e32 v155, v155, v252
	v_mul_f32_e32 v166, v166, v252
	v_mul_f32_e32 v170, v170, v252
	v_mul_f32_e32 v156, v156, v252
	v_mul_f32_e32 v157, v157, v252
	v_mul_f32_e32 v167, v167, v252
	v_mul_f32_e32 v171, v171, v252
	v_mul_f32_e32 v158, v158, v252
	v_mul_f32_e32 v159, v159, v252
	v_mul_f32_e32 v168, v168, v252
	v_mul_f32_e32 v172, v172, v252
	v_mul_f32_e32 v160, v160, v252
	v_mul_f32_e32 v161, v161, v252
	v_mul_f32_e32 v173, v173, v252
	v_mul_f32_e32 v174, v174, v252
	v_mul_f32_e32 v175, v175, v252
	v_mul_f32_e32 v176, v176, v252
	v_mul_f32_e32 v177, v177, v252
	v_mul_f32_e32 v178, v178, v252
	v_mul_f32_e32 v179, v179, v252
	v_mul_f32_e32 v180, v180, v252
	v_mul_f32_e32 v181, v181, v252
	v_mul_f32_e32 v182, v182, v252
	v_mul_f32_e32 v183, v183, v252
	v_mul_f32_e32 v246, v246, v252
	v_mul_f32_e32 v248, v248, v252
	v_mul_f32_e32 v250, v250, v252
	v_mul_f32_e32 v251, v251, v252
	v_mul_f32_e32 v164, v164, v252
	v_mul_f32_e32 v162, v162, v252
	v_mul_f32_e32 v145, v145, v252
	v_sub_f32_e32 v84, v84, v249
	v_sub_f32_e32 v85, v85, v249
	v_sub_f32_e32 v86, v86, v249
	v_sub_f32_e32 v87, v87, v249
	v_sub_f32_e32 v88, v88, v249
	v_sub_f32_e32 v89, v89, v249
	v_sub_f32_e32 v90, v90, v249
	v_sub_f32_e32 v91, v91, v249
	v_sub_f32_e32 v92, v92, v249
	v_sub_f32_e32 v93, v93, v249
	v_sub_f32_e32 v94, v94, v249
	v_sub_f32_e32 v95, v95, v249
	v_sub_f32_e32 v96, v96, v249
	v_sub_f32_e32 v97, v97, v249
	v_sub_f32_e32 v98, v98, v249
	v_sub_f32_e32 v99, v99, v249
	v_sub_f32_e32 v68, v68, v249
	v_sub_f32_e32 v69, v69, v249
	v_sub_f32_e32 v70, v70, v249
	v_sub_f32_e32 v71, v71, v249
	v_sub_f32_e32 v72, v72, v249
	v_sub_f32_e32 v73, v73, v249
	v_sub_f32_e32 v74, v74, v249
	v_sub_f32_e32 v75, v75, v249
	v_sub_f32_e32 v76, v76, v249
	v_sub_f32_e32 v77, v77, v249
	v_sub_f32_e32 v78, v78, v249
	v_sub_f32_e32 v79, v79, v249
	v_sub_f32_e32 v80, v80, v249
	v_sub_f32_e32 v81, v81, v249
	v_sub_f32_e32 v82, v82, v249
	v_sub_f32_e32 v83, v83, v249
	v_sub_f32_e32 v216, v216, v249
	v_sub_f32_e32 v217, v217, v249
	v_sub_f32_e32 v218, v218, v249
	v_sub_f32_e32 v219, v219, v249
	v_sub_f32_e32 v220, v220, v249
	v_sub_f32_e32 v221, v221, v249
	v_sub_f32_e32 v222, v222, v249
	v_sub_f32_e32 v223, v223, v249
	v_sub_f32_e32 v224, v224, v249
	v_sub_f32_e32 v225, v225, v249
	v_sub_f32_e32 v226, v226, v249
	v_sub_f32_e32 v227, v227, v249
	v_sub_f32_e32 v228, v228, v249
	v_sub_f32_e32 v229, v229, v249
	v_sub_f32_e32 v230, v230, v249
	v_sub_f32_e32 v231, v231, v249
	s_and_saveexec_b64 s[10:11], s[6:7]
	ds_write_b32 v184, v252 offset:128
	s_or_b64 exec, exec, s[10:11]
	s_waitcnt lgkmcnt(0)
	v_add_u32_e32 v253, v135, v185
	ds_read_b128 v[212:215], v253 offset:224
	ds_read_b128 v[208:211], v253 offset:192
	ds_read_b128 v[204:207], v253 offset:160
	ds_read_b128 v[200:203], v253 offset:128
	s_waitcnt lgkmcnt(0)
	v_pk_mul_f32 v[52:53], v[52:53], v[200:201]
	v_pk_mul_f32 v[54:55], v[54:55], v[202:203]
	v_pk_mul_f32 v[56:57], v[56:57], v[204:205]
	v_pk_mul_f32 v[58:59], v[58:59], v[206:207]
	v_pk_mul_f32 v[60:61], v[60:61], v[208:209]
	v_pk_mul_f32 v[62:63], v[62:63], v[210:211]
	v_pk_mul_f32 v[64:65], v[64:65], v[212:213]
	v_pk_mul_f32 v[66:67], v[66:67], v[214:215]
	v_pk_mul_f32 v[36:37], v[36:37], v[200:201]
	v_pk_mul_f32 v[38:39], v[38:39], v[202:203]
	v_pk_mul_f32 v[40:41], v[40:41], v[204:205]
	v_pk_mul_f32 v[42:43], v[42:43], v[206:207]
	v_pk_mul_f32 v[44:45], v[44:45], v[208:209]
	v_pk_mul_f32 v[46:47], v[46:47], v[210:211]
	v_pk_mul_f32 v[48:49], v[48:49], v[212:213]
	v_pk_mul_f32 v[50:51], v[50:51], v[214:215]
	v_pk_mul_f32 v[20:21], v[20:21], v[200:201]
	v_pk_mul_f32 v[22:23], v[22:23], v[202:203]
	v_pk_mul_f32 v[24:25], v[24:25], v[204:205]
	v_pk_mul_f32 v[26:27], v[26:27], v[206:207]
	v_pk_mul_f32 v[28:29], v[28:29], v[208:209]
	v_pk_mul_f32 v[30:31], v[30:31], v[210:211]
	v_pk_mul_f32 v[32:33], v[32:33], v[212:213]
	v_pk_mul_f32 v[34:35], v[34:35], v[214:215]
	v_pk_mul_f32 v[4:5], v[4:5], v[200:201]
	v_pk_mul_f32 v[6:7], v[6:7], v[202:203]
	v_pk_mul_f32 v[8:9], v[8:9], v[204:205]
	v_pk_mul_f32 v[10:11], v[10:11], v[206:207]
	v_pk_mul_f32 v[12:13], v[12:13], v[208:209]
	v_pk_mul_f32 v[14:15], v[14:15], v[210:211]
	v_pk_mul_f32 v[16:17], v[16:17], v[212:213]
	v_pk_mul_f32 v[18:19], v[18:19], v[214:215]
	v_cvt_pk_fp8_f32 v232, v165, v169
	v_cvt_pk_fp8_f32 v233, v166, v170
	v_cvt_pk_fp8_f32 v234, v167, v171
	v_cvt_pk_fp8_f32 v235, v168, v172
	v_cvt_pk_fp8_f32 v232, v2, v155 op_sel:[0,0,1]
	v_cvt_pk_fp8_f32 v233, v156, v157 op_sel:[0,0,1]
	v_cvt_pk_fp8_f32 v234, v158, v159 op_sel:[0,0,1]
	v_cvt_pk_fp8_f32 v235, v160, v161 op_sel:[0,0,1]
	v_cvt_pk_fp8_f32 v236, v173, v174
	v_cvt_pk_fp8_f32 v237, v177, v178
	v_cvt_pk_fp8_f32 v238, v181, v182
	v_cvt_pk_fp8_f32 v239, v248, v250
	v_cvt_pk_fp8_f32 v236, v175, v176 op_sel:[0,0,1]
	v_cvt_pk_fp8_f32 v237, v179, v180 op_sel:[0,0,1]
	v_cvt_pk_fp8_f32 v238, v183, v246 op_sel:[0,0,1]
	v_cvt_pk_fp8_f32 v239, v251, v164 op_sel:[0,0,1]
	ds_read_b128 v[208:211], v197 offset:26624
	ds_read_b128 v[212:215], v198 offset:26624
.Lring_norare_b1:
	ds_read_b128 v[200:203], v197 offset:24576
	ds_read_b128 v[204:207], v198 offset:24576
	v_add_f32_e32 v145, v145, v162
	v_exp_f32_e32 v173, v84
	v_exp_f32_e32 v177, v85
	v_exp_f32_e32 v165, v86
	v_exp_f32_e32 v166, v87
	v_exp_f32_e32 v174, v88
	s_waitcnt lgkmcnt(2)
	v_mfma_scale_f32_32x32x64_f8f6f4 v[36:51], v[232:239], v[208:215], v[36:51], v188, v188 op_sel_hi:[0,0,0]
	ds_read_b128 v[208:211], v197 offset:30720
	ds_read_b128 v[212:215], v198 offset:30720
	v_exp_f32_e32 v178, v89
	v_exp_f32_e32 v167, v90
	v_exp_f32_e32 v168, v91
	v_exp_f32_e32 v175, v92
	v_exp_f32_e32 v179, v93
	v_exp_f32_e32 v169, v94
	v_exp_f32_e32 v170, v95
	s_waitcnt lgkmcnt(2)
	v_mfma_scale_f32_32x32x64_f8f6f4 v[52:67], v[232:239], v[200:207], v[52:67], v188, v188 op_sel_hi:[0,0,0]
	ds_read_b128 v[200:203], v197 offset:28672
	ds_read_b128 v[204:207], v198 offset:28672
	v_exp_f32_e32 v176, v96
	v_exp_f32_e32 v180, v97
	v_exp_f32_e32 v171, v98
	v_exp_f32_e32 v172, v99
	v_exp_f32_e32 v154, v68
	v_exp_f32_e32 v155, v69
	v_exp_f32_e32 v130, v70
	s_waitcnt lgkmcnt(2)
	v_mfma_scale_f32_32x32x64_f8f6f4 v[4:19], v[232:239], v[208:215], v[4:19], v188, v188 op_sel_hi:[0,0,0]
	v_exp_f32_e32 v131, v71
	v_exp_f32_e32 v128, v72
	v_exp_f32_e32 v129, v73
	v_exp_f32_e32 v126, v74
	v_exp_f32_e32 v127, v75
	v_exp_f32_e32 v124, v76
	v_exp_f32_e32 v125, v77
	s_waitcnt lgkmcnt(0)
	v_mfma_scale_f32_32x32x64_f8f6f4 v[20:35], v[232:239], v[200:207], v[20:35], v188, v188 op_sel_hi:[0,0,0]
	v_exp_f32_e32 v160, v78
	v_exp_f32_e32 v161, v79
	v_exp_f32_e32 v158, v80
	v_exp_f32_e32 v159, v81
	v_exp_f32_e32 v156, v82
	v_exp_f32_e32 v157, v83
	s_add_i32 s15, s15, 2
	v_lshl_add_u64 v[150:151], v[150:151], 0, s[28:29]
	v_add_u32_e32 v152, 0x4000, v152
	s_and_b64 vcc, exec, s[8:9]
	s_waitcnt lgkmcnt(0)
	s_barrier
	s_cbranch_vccnz .LBB0_421
	s_branch .LBB0_409
